# v63 plus publisher wave writes copy B with 16-byte sc1 stores (16 lanes) instead of 8-byte stores (32 lanes)
# speedup vs baseline: 1.0026x; 1.0026x over previous
_Z11lstm_kernelPKDF16_PKDv8_DF16_S3_S3_PKfS5_S5_S5_PDF16_S6_PfS5_PS1_PK15HIP_vector_typeIfLj4EES5_S5_S7_S5_S5_S5_:
	s_load_dwordx16 s[8:23], s[0:1], 0x40
	s_and_b32 s3, s2, 7
	s_ashr_i32 s33, s2, 3
	s_cmp_lt_u32 s3, 2
	s_mov_b64 s[4:5], -1
	s_cbranch_scc0 .LBB0_68
	v_cmp_gt_u32_e32 vcc, 40, v0
	s_and_saveexec_b64 s[4:5], vcc
	v_lshl_add_u32 v1, v0, 2, 0
	v_mov_b32_e32 v2, 0
	ds_write_b32 v1, v2 offset:61440
	s_or_b64 exec, exec, s[4:5]
	s_load_dwordx16 s[36:51], s[0:1], 0x0
	v_and_b32_e32 v130, 63, v0
	v_cmp_lt_u32_e32 vcc, 63, v0
	s_waitcnt lgkmcnt(0)
	s_barrier
	s_and_saveexec_b64 s[4:5], vcc
	s_xor_b64 s[24:25], exec, s[4:5]
	s_cbranch_execz .LBB0_33
	s_movk_i32 s4, 0xbf
	v_cmp_lt_u32_e32 vcc, s4, v0
	s_and_saveexec_b64 s[4:5], vcc
	s_xor_b64 s[6:7], exec, s[4:5]
	s_cbranch_execz .LBB0_11
	s_cmp_eq_u32 s3, 0
	s_cselect_b64 s[26:27], -1, 0
	s_lshl_b32 s28, s33, 7
	s_ashr_i32 s29, s28, 31
	s_lshl_b64 s[28:29], s[28:29], 1
	s_add_u32 s28, s10, s28
	v_lshlrev_b32_e32 v2, 4, v0
	v_mov_b32_e32 v3, 0
	s_addc_u32 s29, s11, s29
	v_and_b32_e32 v2, 0xf0, v2
	v_lshl_add_u64 v[4:5], s[28:29], 0, v[2:3]
	v_lshrrev_b32_e32 v2, 1, v0
	v_and_b32_e32 v2, 8, v2
	s_mov_b32 s30, 0
	v_lshl_add_u32 v1, v130, 3, 0
	v_cmp_gt_u32_e64 s[4:5], 16, v130
	v_lshl_add_u64 v[4:5], v[4:5], 0, v[2:3]
	s_branch .LBB0_7

.LBB0_9:
	s_and_saveexec_b64 s[28:29], s[4:5]
	s_cbranch_execz .LBB0_6
	s_cmp_gt_u32 s30, 29
	s_cselect_b32 s31, 0xffffffe2, 0
	s_cselect_b32 s52, 2, 0
	s_add_i32 s31, s31, s30
	s_sub_i32 s53, 29, s31
	s_and_b64 s[34:35], s[26:27], exec
	v_lshl_add_u32 v2, s31, 8, v1
	s_cselect_b32 s31, s31, s53
	s_or_b32 s34, s52, s3
	ds_read_b64 v[6:7], v2 offset:61696
	ds_read_b64 v[8:9], v2 offset:61824
	s_mul_i32 s34, s34, 30
	s_add_i32 s34, s31, s34
	s_ashr_i32 s35, s34, 31
	s_lshl_b64 s[34:35], s[34:35], 13
	v_lshl_add_u64 v[10:11], v[4:5], 0, s[34:35]
	s_waitcnt lgkmcnt(0)
	global_store_dwordx4 v[10:11], v[6:9], off sc1
	s_branch .LBB0_6
